# speedup vs baseline: 1.0776x; 1.0004x over previous
_Z15qkv_proj_kernelPKDF16_S0_PKfS2_S2_PDF16_S3_S3_:
	s_lshr_b32 s4, s2, 2
	s_and_b32 s3, s2, 7
	s_and_b32 s22, s4, 8
	s_or_b32 s4, s22, s3
	v_readfirstlane_b32 s18, v0
	s_ashr_i32 s3, s2, 6
	s_lshl_b32 s21, s4, 8
	s_bfe_u32 s20, s2, 0x20003
	v_and_b32_e32 v1, 63, v0
	s_cmpk_lt_u32 s18, 0x200
	s_mulk_i32 s20, 0xc0
	s_cbranch_scc1 .LBB1_30
	s_load_dwordx4 s[4:7], s[0:1], 0x0
	s_sub_i32 s10, 2, s3
	s_lshr_b32 s12, s18, 6
	s_add_i32 s12, s12, -8
	s_mul_i32 s13, s10, 0x600000
	s_mul_hi_i32 s14, s10, 0x600000
	s_mul_i32 s15, s10, 0x120000
	s_waitcnt lgkmcnt(0)
	s_add_u32 s4, s4, s13
	s_addc_u32 s5, s5, s14
	s_add_u32 s6, s6, s15
	s_addc_u32 s7, s7, 0
	v_lshrrev_b32_e32 v2, 2, v1
	v_lshrrev_b32_e32 v3, 4, v1
	v_xor_b32_e32 v3, v3, v1
	v_and_b32_e32 v3, 3, v3
	v_lshlrev_b32_e32 v3, 4, v3
	v_mul_u32_u24_e32 v2, 0x600, v2
	v_add_u32_e32 v2, v2, v3
	s_mul_i32 s16, s12, 7
	s_mul_i32 s27, s20, 0x600
	s_add_u32 s6, s6, s27
	s_addc_u32 s7, s7, 0
	s_add_i32 s27, s21, -192
	s_mul_i32 s27, s27, 0x600
	s_ashr_i32 s28, s27, 31
	s_add_u32 s4, s4, s27
	s_addc_u32 s5, s5, s28
	s_add_i32 s17, s16, 0
	s_cmp_ge_u32 s17, 12
	s_cselect_b32 s24, s4, s6
	s_cselect_b32 s25, s5, s7
	s_mul_i32 s17, s17, 0x6000
	s_add_u32 s30, s24, s17
	s_addc_u32 s31, s25, 0
	s_add_i32 s17, s16, 1
	s_cmp_ge_u32 s17, 12
	s_cselect_b32 s24, s4, s6
	s_cselect_b32 s25, s5, s7
	s_mul_i32 s17, s17, 0x6000
	s_add_u32 s32, s24, s17
	s_addc_u32 s33, s25, 0
	s_add_i32 s17, s16, 2
	s_cmp_ge_u32 s17, 12
	s_cselect_b32 s24, s4, s6
	s_cselect_b32 s25, s5, s7
	s_mul_i32 s17, s17, 0x6000
	s_add_u32 s34, s24, s17
	s_addc_u32 s35, s25, 0
	s_add_i32 s17, s16, 3
	s_cmp_ge_u32 s17, 12
	s_cselect_b32 s24, s4, s6
	s_cselect_b32 s25, s5, s7
	s_mul_i32 s17, s17, 0x6000
	s_add_u32 s36, s24, s17
	s_addc_u32 s37, s25, 0
	s_add_i32 s17, s16, 4
	s_cmp_ge_u32 s17, 12
	s_cselect_b32 s24, s4, s6
	s_cselect_b32 s25, s5, s7
	s_mul_i32 s17, s17, 0x6000
	s_add_u32 s38, s24, s17
	s_addc_u32 s39, s25, 0
	s_add_i32 s17, s16, 5
	s_cmp_ge_u32 s17, 12
	s_cselect_b32 s24, s4, s6
	s_cselect_b32 s25, s5, s7
	s_mul_i32 s17, s17, 0x6000
	s_add_u32 s40, s24, s17
	s_addc_u32 s41, s25, 0
	s_add_i32 s17, s16, 6
	s_cmp_ge_u32 s17, 12
	s_cselect_b32 s24, s4, s6
	s_cselect_b32 s25, s5, s7
	s_mul_i32 s17, s17, 0x6000
	s_add_u32 s42, s24, s17
	s_addc_u32 s43, s25, 0
	s_mul_i32 s26, s12, 0x1c00
	s_add_i32 m0, s26, 2048
	s_nop 0
	global_load_lds_dwordx4 v2, s[30:31]
	s_add_i32 m0, s26, 3072
	s_nop 0
	global_load_lds_dwordx4 v2, s[32:33]
	s_add_i32 m0, s26, 4096
	s_nop 0
	global_load_lds_dwordx4 v2, s[34:35]
	s_add_i32 m0, s26, 5120
	s_nop 0
	global_load_lds_dwordx4 v2, s[36:37]
	s_add_i32 m0, s26, 6144
	s_nop 0
	global_load_lds_dwordx4 v2, s[38:39]
	s_add_i32 m0, s26, 7168
	s_nop 0
	global_load_lds_dwordx4 v2, s[40:41]
	s_add_i32 m0, s26, 8192
	s_nop 0
	global_load_lds_dwordx4 v2, s[42:43]
	s_add_i32 m0, s26, 30656
	s_nop 0
	global_load_lds_dwordx4 v2, s[30:31] offset:64
	s_add_i32 m0, s26, 31680
	s_nop 0
	global_load_lds_dwordx4 v2, s[32:33] offset:64
	s_add_i32 m0, s26, 32704
	s_nop 0
	global_load_lds_dwordx4 v2, s[34:35] offset:64
	s_add_i32 m0, s26, 33728
	s_nop 0
	global_load_lds_dwordx4 v2, s[36:37] offset:64
	s_add_i32 m0, s26, 34752
	s_nop 0
	global_load_lds_dwordx4 v2, s[38:39] offset:64
	s_add_i32 m0, s26, 35776
	s_nop 0
	global_load_lds_dwordx4 v2, s[40:41] offset:64
	s_add_i32 m0, s26, 36800
	s_nop 0
	global_load_lds_dwordx4 v2, s[42:43] offset:64
	s_add_i32 m0, s26, 59264
	s_nop 0
	global_load_lds_dwordx4 v2, s[30:31] offset:128
	s_add_i32 m0, s26, 60288
	s_nop 0
	global_load_lds_dwordx4 v2, s[32:33] offset:128
	s_add_i32 m0, s26, 61312
	s_nop 0
	global_load_lds_dwordx4 v2, s[34:35] offset:128
	s_add_i32 m0, s26, 62336
	s_nop 0
	global_load_lds_dwordx4 v2, s[36:37] offset:128
	s_add_i32 m0, s26, 63360
	s_nop 0
	global_load_lds_dwordx4 v2, s[38:39] offset:128
	s_add_i32 m0, s26, 64384
	s_nop 0
	global_load_lds_dwordx4 v2, s[40:41] offset:128
	s_add_i32 m0, s26, 65408
	s_nop 0
	global_load_lds_dwordx4 v2, s[42:43] offset:128
	s_add_i32 m0, s26, 87872
	s_nop 0
	global_load_lds_dwordx4 v2, s[30:31] offset:192
	s_add_i32 m0, s26, 88896
	s_nop 0
	global_load_lds_dwordx4 v2, s[32:33] offset:192
	s_add_i32 m0, s26, 89920
	s_nop 0
	global_load_lds_dwordx4 v2, s[34:35] offset:192
	s_add_i32 m0, s26, 90944
	s_nop 0
	global_load_lds_dwordx4 v2, s[36:37] offset:192
	s_add_i32 m0, s26, 91968
	s_nop 0
	global_load_lds_dwordx4 v2, s[38:39] offset:192
	s_add_i32 m0, s26, 92992
	s_nop 0
	global_load_lds_dwordx4 v2, s[40:41] offset:192
	s_add_i32 m0, s26, 94016
	s_nop 0
	global_load_lds_dwordx4 v2, s[42:43] offset:192
	s_waitcnt vmcnt(21)
	s_barrier
	s_add_i32 m0, s26, 116480
	s_nop 0
	global_load_lds_dwordx4 v2, s[30:31] offset:256
	s_add_i32 m0, s26, 117504
	s_nop 0
	global_load_lds_dwordx4 v2, s[32:33] offset:256
	s_add_i32 m0, s26, 118528
	s_nop 0
	global_load_lds_dwordx4 v2, s[34:35] offset:256
	s_add_i32 m0, s26, 119552
	s_nop 0
	global_load_lds_dwordx4 v2, s[36:37] offset:256
	s_add_i32 m0, s26, 120576
	s_nop 0
	global_load_lds_dwordx4 v2, s[38:39] offset:256
	s_add_i32 m0, s26, 121600
	s_nop 0
	global_load_lds_dwordx4 v2, s[40:41] offset:256
	s_add_i32 m0, s26, 122624
	s_nop 0
	global_load_lds_dwordx4 v2, s[42:43] offset:256
	s_waitcnt vmcnt(21)
	s_barrier
	s_add_i32 m0, s26, 1728
	s_nop 0
	global_load_lds_dwordx4 v2, s[30:31] offset:320
	s_add_i32 m0, s26, 2752
	s_nop 0
	global_load_lds_dwordx4 v2, s[32:33] offset:320
	s_add_i32 m0, s26, 3776
	s_nop 0
	global_load_lds_dwordx4 v2, s[34:35] offset:320
	s_add_i32 m0, s26, 4800
	s_nop 0
	global_load_lds_dwordx4 v2, s[36:37] offset:320
	s_add_i32 m0, s26, 5824
	s_nop 0
	global_load_lds_dwordx4 v2, s[38:39] offset:320
	s_add_i32 m0, s26, 6848
	s_nop 0
	global_load_lds_dwordx4 v2, s[40:41] offset:320
	s_add_i32 m0, s26, 7872
	s_nop 0
	global_load_lds_dwordx4 v2, s[42:43] offset:320
	s_waitcnt vmcnt(21)
	s_barrier
	s_add_i32 m0, s26, 30336
	s_nop 0
	global_load_lds_dwordx4 v2, s[30:31] offset:384
	s_add_i32 m0, s26, 31360
	s_nop 0
	global_load_lds_dwordx4 v2, s[32:33] offset:384
	s_add_i32 m0, s26, 32384
	s_nop 0
	global_load_lds_dwordx4 v2, s[34:35] offset:384
	s_add_i32 m0, s26, 33408
	s_nop 0
	global_load_lds_dwordx4 v2, s[36:37] offset:384
	s_add_i32 m0, s26, 34432
	s_nop 0
	global_load_lds_dwordx4 v2, s[38:39] offset:384
	s_add_i32 m0, s26, 35456
	s_nop 0
	global_load_lds_dwordx4 v2, s[40:41] offset:384
	s_add_i32 m0, s26, 36480
	s_nop 0
	global_load_lds_dwordx4 v2, s[42:43] offset:384
	s_waitcnt vmcnt(21)
	s_barrier
	s_add_i32 m0, s26, 58944
	s_nop 0
	global_load_lds_dwordx4 v2, s[30:31] offset:448
	s_add_i32 m0, s26, 59968
	s_nop 0
	global_load_lds_dwordx4 v2, s[32:33] offset:448
	s_add_i32 m0, s26, 60992
	s_nop 0
	global_load_lds_dwordx4 v2, s[34:35] offset:448
	s_add_i32 m0, s26, 62016
	s_nop 0
	global_load_lds_dwordx4 v2, s[36:37] offset:448
	s_add_i32 m0, s26, 63040
	s_nop 0
	global_load_lds_dwordx4 v2, s[38:39] offset:448
	s_add_i32 m0, s26, 64064
	s_nop 0
	global_load_lds_dwordx4 v2, s[40:41] offset:448
	s_add_i32 m0, s26, 65088
	s_nop 0
	global_load_lds_dwordx4 v2, s[42:43] offset:448
	s_waitcnt vmcnt(21)
	s_barrier
	s_add_i32 m0, s26, 87552
	s_nop 0
	global_load_lds_dwordx4 v2, s[30:31] offset:512
	s_add_i32 m0, s26, 88576
	s_nop 0
	global_load_lds_dwordx4 v2, s[32:33] offset:512
	s_add_i32 m0, s26, 89600
	s_nop 0
	global_load_lds_dwordx4 v2, s[34:35] offset:512
	s_add_i32 m0, s26, 90624
	s_nop 0
	global_load_lds_dwordx4 v2, s[36:37] offset:512
	s_add_i32 m0, s26, 91648
	s_nop 0
	global_load_lds_dwordx4 v2, s[38:39] offset:512
	s_add_i32 m0, s26, 92672
	s_nop 0
	global_load_lds_dwordx4 v2, s[40:41] offset:512
	s_add_i32 m0, s26, 93696
	s_nop 0
	global_load_lds_dwordx4 v2, s[42:43] offset:512
	s_waitcnt vmcnt(21)
	s_barrier
	s_add_i32 m0, s26, 116160
	s_nop 0
	global_load_lds_dwordx4 v2, s[30:31] offset:576
	s_add_i32 m0, s26, 117184
	s_nop 0
	global_load_lds_dwordx4 v2, s[32:33] offset:576
	s_add_i32 m0, s26, 118208
	s_nop 0
	global_load_lds_dwordx4 v2, s[34:35] offset:576
	s_add_i32 m0, s26, 119232
	s_nop 0
	global_load_lds_dwordx4 v2, s[36:37] offset:576
	s_add_i32 m0, s26, 120256
	s_nop 0
	global_load_lds_dwordx4 v2, s[38:39] offset:576
	s_add_i32 m0, s26, 121280
	s_nop 0
	global_load_lds_dwordx4 v2, s[40:41] offset:576
	s_add_i32 m0, s26, 122304
	s_nop 0
	global_load_lds_dwordx4 v2, s[42:43] offset:576
	s_waitcnt vmcnt(21)
	s_barrier
	s_add_i32 m0, s26, 1408
	s_nop 0
	global_load_lds_dwordx4 v2, s[30:31] offset:640
	s_add_i32 m0, s26, 2432
	s_nop 0
	global_load_lds_dwordx4 v2, s[32:33] offset:640
	s_add_i32 m0, s26, 3456
	s_nop 0
	global_load_lds_dwordx4 v2, s[34:35] offset:640
	s_add_i32 m0, s26, 4480
	s_nop 0
	global_load_lds_dwordx4 v2, s[36:37] offset:640
	s_add_i32 m0, s26, 5504
	s_nop 0
	global_load_lds_dwordx4 v2, s[38:39] offset:640
	s_add_i32 m0, s26, 6528
	s_nop 0
	global_load_lds_dwordx4 v2, s[40:41] offset:640
	s_add_i32 m0, s26, 7552
	s_nop 0
	global_load_lds_dwordx4 v2, s[42:43] offset:640
	s_waitcnt vmcnt(21)
	s_barrier
	s_add_i32 m0, s26, 30016
	s_nop 0
	global_load_lds_dwordx4 v2, s[30:31] offset:704
	s_add_i32 m0, s26, 31040
	s_nop 0
	global_load_lds_dwordx4 v2, s[32:33] offset:704
	s_add_i32 m0, s26, 32064
	s_nop 0
	global_load_lds_dwordx4 v2, s[34:35] offset:704
	s_add_i32 m0, s26, 33088
	s_nop 0
	global_load_lds_dwordx4 v2, s[36:37] offset:704
	s_add_i32 m0, s26, 34112
	s_nop 0
	global_load_lds_dwordx4 v2, s[38:39] offset:704
	s_add_i32 m0, s26, 35136
	s_nop 0
	global_load_lds_dwordx4 v2, s[40:41] offset:704
	s_add_i32 m0, s26, 36160
	s_nop 0
	global_load_lds_dwordx4 v2, s[42:43] offset:704
	s_waitcnt vmcnt(21)
	s_barrier
	s_add_i32 m0, s26, 58624
	s_nop 0
	global_load_lds_dwordx4 v2, s[30:31] offset:768
	s_add_i32 m0, s26, 59648
	s_nop 0
	global_load_lds_dwordx4 v2, s[32:33] offset:768
	s_add_i32 m0, s26, 60672
	s_nop 0
	global_load_lds_dwordx4 v2, s[34:35] offset:768
	s_add_i32 m0, s26, 61696
	s_nop 0
	global_load_lds_dwordx4 v2, s[36:37] offset:768
	s_add_i32 m0, s26, 62720
	s_nop 0
	global_load_lds_dwordx4 v2, s[38:39] offset:768
	s_add_i32 m0, s26, 63744
	s_nop 0
	global_load_lds_dwordx4 v2, s[40:41] offset:768
	s_add_i32 m0, s26, 64768
	s_nop 0
	global_load_lds_dwordx4 v2, s[42:43] offset:768
	s_waitcnt vmcnt(21)
	s_barrier
	s_add_i32 m0, s26, 87232
	s_nop 0
	global_load_lds_dwordx4 v2, s[30:31] offset:832
	s_add_i32 m0, s26, 88256
	s_nop 0
	global_load_lds_dwordx4 v2, s[32:33] offset:832
	s_add_i32 m0, s26, 89280
	s_nop 0
	global_load_lds_dwordx4 v2, s[34:35] offset:832
	s_add_i32 m0, s26, 90304
	s_nop 0
	global_load_lds_dwordx4 v2, s[36:37] offset:832
	s_add_i32 m0, s26, 91328
	s_nop 0
	global_load_lds_dwordx4 v2, s[38:39] offset:832
	s_add_i32 m0, s26, 92352
	s_nop 0
	global_load_lds_dwordx4 v2, s[40:41] offset:832
	s_add_i32 m0, s26, 93376
	s_nop 0
	global_load_lds_dwordx4 v2, s[42:43] offset:832
	s_waitcnt vmcnt(21)
	s_barrier
	s_add_i32 m0, s26, 115840
	s_nop 0
	global_load_lds_dwordx4 v2, s[30:31] offset:896
	s_add_i32 m0, s26, 116864
	s_nop 0
	global_load_lds_dwordx4 v2, s[32:33] offset:896
	s_add_i32 m0, s26, 117888
	s_nop 0
	global_load_lds_dwordx4 v2, s[34:35] offset:896
	s_add_i32 m0, s26, 118912
	s_nop 0
	global_load_lds_dwordx4 v2, s[36:37] offset:896
	s_add_i32 m0, s26, 119936
	s_nop 0
	global_load_lds_dwordx4 v2, s[38:39] offset:896
	s_add_i32 m0, s26, 120960
	s_nop 0
	global_load_lds_dwordx4 v2, s[40:41] offset:896
	s_add_i32 m0, s26, 121984
	s_nop 0
	global_load_lds_dwordx4 v2, s[42:43] offset:896
	s_waitcnt vmcnt(21)
	s_barrier
	s_add_i32 m0, s26, 1088
	s_nop 0
	global_load_lds_dwordx4 v2, s[30:31] offset:960
	s_add_i32 m0, s26, 2112
	s_nop 0
	global_load_lds_dwordx4 v2, s[32:33] offset:960
	s_add_i32 m0, s26, 3136
	s_nop 0
	global_load_lds_dwordx4 v2, s[34:35] offset:960
	s_add_i32 m0, s26, 4160
	s_nop 0
	global_load_lds_dwordx4 v2, s[36:37] offset:960
	s_add_i32 m0, s26, 5184
	s_nop 0
	global_load_lds_dwordx4 v2, s[38:39] offset:960
	s_add_i32 m0, s26, 6208
	s_nop 0
	global_load_lds_dwordx4 v2, s[40:41] offset:960
	s_add_i32 m0, s26, 7232
	s_nop 0
	global_load_lds_dwordx4 v2, s[42:43] offset:960
	s_waitcnt vmcnt(21)
	s_barrier
	s_add_i32 m0, s26, 29696
	s_nop 0
	global_load_lds_dwordx4 v2, s[30:31] offset:1024
	s_add_i32 m0, s26, 30720
	s_nop 0
	global_load_lds_dwordx4 v2, s[32:33] offset:1024
	s_add_i32 m0, s26, 31744
	s_nop 0
	global_load_lds_dwordx4 v2, s[34:35] offset:1024
	s_add_i32 m0, s26, 32768
	s_nop 0
	global_load_lds_dwordx4 v2, s[36:37] offset:1024
	s_add_i32 m0, s26, 33792
	s_nop 0
	global_load_lds_dwordx4 v2, s[38:39] offset:1024
	s_add_i32 m0, s26, 34816
	s_nop 0
	global_load_lds_dwordx4 v2, s[40:41] offset:1024
	s_add_i32 m0, s26, 35840
	s_nop 0
	global_load_lds_dwordx4 v2, s[42:43] offset:1024
	s_waitcnt vmcnt(21)
	s_barrier
	s_add_i32 m0, s26, 58304
	s_nop 0
	global_load_lds_dwordx4 v2, s[30:31] offset:1088
	s_add_i32 m0, s26, 59328
	s_nop 0
	global_load_lds_dwordx4 v2, s[32:33] offset:1088
	s_add_i32 m0, s26, 60352
	s_nop 0
	global_load_lds_dwordx4 v2, s[34:35] offset:1088
	s_add_i32 m0, s26, 61376
	s_nop 0
	global_load_lds_dwordx4 v2, s[36:37] offset:1088
	s_add_i32 m0, s26, 62400
	s_nop 0
	global_load_lds_dwordx4 v2, s[38:39] offset:1088
	s_add_i32 m0, s26, 63424
	s_nop 0
	global_load_lds_dwordx4 v2, s[40:41] offset:1088
	s_add_i32 m0, s26, 64448
	s_nop 0
	global_load_lds_dwordx4 v2, s[42:43] offset:1088
	s_waitcnt vmcnt(21)
	s_barrier
	s_add_i32 m0, s26, 86912
	s_nop 0
	global_load_lds_dwordx4 v2, s[30:31] offset:1152
	s_add_i32 m0, s26, 87936
	s_nop 0
	global_load_lds_dwordx4 v2, s[32:33] offset:1152
	s_add_i32 m0, s26, 88960
	s_nop 0
	global_load_lds_dwordx4 v2, s[34:35] offset:1152
	s_add_i32 m0, s26, 89984
	s_nop 0
	global_load_lds_dwordx4 v2, s[36:37] offset:1152
	s_add_i32 m0, s26, 91008
	s_nop 0
	global_load_lds_dwordx4 v2, s[38:39] offset:1152
	s_add_i32 m0, s26, 92032
	s_nop 0
	global_load_lds_dwordx4 v2, s[40:41] offset:1152
	s_add_i32 m0, s26, 93056
	s_nop 0
	global_load_lds_dwordx4 v2, s[42:43] offset:1152
	s_waitcnt vmcnt(21)
	s_barrier
	s_add_i32 m0, s26, 115520
	s_nop 0
	global_load_lds_dwordx4 v2, s[30:31] offset:1216
	s_add_i32 m0, s26, 116544
	s_nop 0
	global_load_lds_dwordx4 v2, s[32:33] offset:1216
	s_add_i32 m0, s26, 117568
	s_nop 0
	global_load_lds_dwordx4 v2, s[34:35] offset:1216
	s_add_i32 m0, s26, 118592
	s_nop 0
	global_load_lds_dwordx4 v2, s[36:37] offset:1216
	s_add_i32 m0, s26, 119616
	s_nop 0
	global_load_lds_dwordx4 v2, s[38:39] offset:1216
	s_add_i32 m0, s26, 120640
	s_nop 0
	global_load_lds_dwordx4 v2, s[40:41] offset:1216
	s_add_i32 m0, s26, 121664
	s_nop 0
	global_load_lds_dwordx4 v2, s[42:43] offset:1216
	s_waitcnt vmcnt(21)
	s_barrier
	s_add_i32 m0, s26, 768
	s_nop 0
	global_load_lds_dwordx4 v2, s[30:31] offset:1280
	s_add_i32 m0, s26, 1792
	s_nop 0
	global_load_lds_dwordx4 v2, s[32:33] offset:1280
	s_add_i32 m0, s26, 2816
	s_nop 0
	global_load_lds_dwordx4 v2, s[34:35] offset:1280
	s_add_i32 m0, s26, 3840
	s_nop 0
	global_load_lds_dwordx4 v2, s[36:37] offset:1280
	s_add_i32 m0, s26, 4864
	s_nop 0
	global_load_lds_dwordx4 v2, s[38:39] offset:1280
	s_add_i32 m0, s26, 5888
	s_nop 0
	global_load_lds_dwordx4 v2, s[40:41] offset:1280
	s_add_i32 m0, s26, 6912
	s_nop 0
	global_load_lds_dwordx4 v2, s[42:43] offset:1280
	s_waitcnt vmcnt(21)
	s_barrier
	s_add_i32 m0, s26, 29376
	s_nop 0
	global_load_lds_dwordx4 v2, s[30:31] offset:1344
	s_add_i32 m0, s26, 30400
	s_nop 0
	global_load_lds_dwordx4 v2, s[32:33] offset:1344
	s_add_i32 m0, s26, 31424
	s_nop 0
	global_load_lds_dwordx4 v2, s[34:35] offset:1344
	s_add_i32 m0, s26, 32448
	s_nop 0
	global_load_lds_dwordx4 v2, s[36:37] offset:1344
	s_add_i32 m0, s26, 33472
	s_nop 0
	global_load_lds_dwordx4 v2, s[38:39] offset:1344
	s_add_i32 m0, s26, 34496
	s_nop 0
	global_load_lds_dwordx4 v2, s[40:41] offset:1344
	s_add_i32 m0, s26, 35520
	s_nop 0
	global_load_lds_dwordx4 v2, s[42:43] offset:1344
	s_waitcnt vmcnt(21)
	s_barrier
	s_add_i32 m0, s26, 57984
	s_nop 0
	global_load_lds_dwordx4 v2, s[30:31] offset:1408
	s_add_i32 m0, s26, 59008
	s_nop 0
	global_load_lds_dwordx4 v2, s[32:33] offset:1408
	s_add_i32 m0, s26, 60032
	s_nop 0
	global_load_lds_dwordx4 v2, s[34:35] offset:1408
	s_add_i32 m0, s26, 61056
	s_nop 0
	global_load_lds_dwordx4 v2, s[36:37] offset:1408
	s_add_i32 m0, s26, 62080
	s_nop 0
	global_load_lds_dwordx4 v2, s[38:39] offset:1408
	s_add_i32 m0, s26, 63104
	s_nop 0
	global_load_lds_dwordx4 v2, s[40:41] offset:1408
	s_add_i32 m0, s26, 64128
	s_nop 0
	global_load_lds_dwordx4 v2, s[42:43] offset:1408
	s_waitcnt vmcnt(21)
	s_barrier
	s_add_i32 m0, s26, 86592
	s_nop 0
	global_load_lds_dwordx4 v2, s[30:31] offset:1472
	s_add_i32 m0, s26, 87616
	s_nop 0
	global_load_lds_dwordx4 v2, s[32:33] offset:1472
	s_add_i32 m0, s26, 88640
	s_nop 0
	global_load_lds_dwordx4 v2, s[34:35] offset:1472
	s_add_i32 m0, s26, 89664
	s_nop 0
	global_load_lds_dwordx4 v2, s[36:37] offset:1472
	s_add_i32 m0, s26, 90688
	s_nop 0
	global_load_lds_dwordx4 v2, s[38:39] offset:1472
	s_add_i32 m0, s26, 91712
	s_nop 0
	global_load_lds_dwordx4 v2, s[40:41] offset:1472
	s_add_i32 m0, s26, 92736
	s_nop 0
	global_load_lds_dwordx4 v2, s[42:43] offset:1472
	s_waitcnt vmcnt(21)
	s_barrier
	s_waitcnt vmcnt(14)
	s_barrier
	s_waitcnt vmcnt(7)
	s_barrier
	s_waitcnt vmcnt(0)
	s_barrier

	.amdhsa_kernel _Z15qkv_proj_kernelPKDF16_S0_PKfS2_S2_PDF16_S3_S3_
		.amdhsa_group_segment_fixed_size 30720
		.amdhsa_private_segment_fixed_size 0
		.amdhsa_kernarg_size 64
		.amdhsa_user_sgpr_count 2
		.amdhsa_user_sgpr_dispatch_ptr 0
		.amdhsa_user_sgpr_queue_ptr 0
		.amdhsa_user_sgpr_kernarg_segment_ptr 1
		.amdhsa_user_sgpr_dispatch_id 0
		.amdhsa_user_sgpr_kernarg_preload_length 0
		.amdhsa_user_sgpr_kernarg_preload_offset 0
		.amdhsa_user_sgpr_private_segment_size 0
		.amdhsa_uses_dynamic_stack 0
		.amdhsa_enable_private_segment 0
		.amdhsa_system_sgpr_workgroup_id_x 1
		.amdhsa_system_sgpr_workgroup_id_y 0
		.amdhsa_system_sgpr_workgroup_id_z 0
		.amdhsa_system_sgpr_workgroup_info 0
		.amdhsa_system_vgpr_workitem_id 0
		.amdhsa_next_free_vgpr 156
		.amdhsa_next_free_sgpr 46
		.amdhsa_accum_offset 156
		.amdhsa_reserve_vcc 1
		.amdhsa_float_round_mode_32 0
		.amdhsa_float_round_mode_16_64 0
		.amdhsa_float_denorm_mode_32 3
		.amdhsa_float_denorm_mode_16_64 3
		.amdhsa_dx10_clamp 1
		.amdhsa_ieee_mode 1
		.amdhsa_fp16_overflow 0
		.amdhsa_tg_split 0
		.amdhsa_exception_fp_ieee_invalid_op 0
		.amdhsa_exception_fp_denorm_src 0
		.amdhsa_exception_fp_ieee_div_zero 0
		.amdhsa_exception_fp_ieee_overflow 0
		.amdhsa_exception_fp_ieee_underflow 0
		.amdhsa_exception_fp_ieee_inexact 0
		.amdhsa_exception_int_div_zero 0
	.end_amdhsa_kernel

_Z11attn_kernelPKDF16_S0_S0_PDF16_P15HIP_vector_typeIfLj2EE:
	s_mov_b32 s28, s2
	s_load_dwordx4 s[32:35], s[0:1], 0x8
	v_readfirstlane_b32 s3, v0
	s_ashr_i32 s12, s2, 5
	s_lshr_b32 s21, s3, 6
	s_and_b32 s3, s2, 7
	s_and_b32 s12, s12, -8
	s_load_dwordx8 s[4:11], s[0:1], 0x0
	s_or_b32 s12, s12, s3
	s_bfe_u32 s20, s2, 0x10003
	s_lshl_b32 s2, s2, 3
	s_and_b32 s2, s2, 0x780
	s_lshl_b32 s3, s21, 5
	s_ashr_i32 s13, s12, 31
	s_add_i32 s2, s3, s2
	s_lshl_b64 s[16:17], s[12:13], 11
	s_lshl_b32 s3, s20, 10
	s_or_b32 s14, s16, s3
	s_mov_b32 s15, s17
	s_lshl_b64 s[18:19], s[14:15], 7
	s_lshl_b64 s[14:15], s[12:13], 18
	s_waitcnt lgkmcnt(0)
	s_add_u32 s3, s8, s14
	s_addc_u32 s22, s9, s15
	s_add_u32 s16, s16, s2
	v_and_b32_e32 v98, 31, v0
	s_addc_u32 s17, s17, 0
	v_or_b32_e32 v2, s16, v98
	v_mov_b32_e32 v3, s17
	v_bfe_u32 v54, v0, 5, 1
	v_lshlrev_b64 v[2:3], 7, v[2:3]
	v_mov_b32_e32 v51, 0
	v_lshl_add_u64 v[2:3], s[4:5], 0, v[2:3]
	v_lshlrev_b32_e32 v50, 4, v54
	v_lshl_add_u64 v[2:3], v[2:3], 0, v[50:51]
	s_add_u32 s18, s6, s18
	v_bfe_u32 v1, v0, 3, 3
	global_load_dwordx4 v[94:97], v[2:3], off nt
	global_load_dwordx4 v[90:93], v[2:3], off offset:32 nt
	global_load_dwordx4 v[86:89], v[2:3], off offset:64 nt
	global_load_dwordx4 v[82:85], v[2:3], off offset:96 nt
	s_addc_u32 s19, s7, s19
	s_lshl_b32 s24, s20, 11
	v_lshl_or_b32 v2, s21, 4, v1
	v_and_b32_e32 v99, 63, v0
	s_add_u32 s4, s3, s24
	v_or_b32_e32 v3, 8, v2
	v_lshlrev_b32_e32 v4, 4, v0
	s_movk_i32 s3, 0x70
	v_bitop3_b32 v53, v99, s3, v4 bitop3:0x48
	v_lshrrev_b32_e32 v4, 1, v3
	v_xor_b32_e32 v4, v4, v0
	s_addc_u32 s5, s22, 0
	v_lshlrev_b32_e32 v4, 4, v4
	s_lshl_b32 s22, s21, 11
	v_and_b32_e32 v52, 0x70, v4
	v_lshl_or_b32 v55, v2, 7, v53
	s_mov_b32 m0, s22
	v_lshl_or_b32 v64, v3, 7, v52
	global_load_lds_dwordx4 v55, s[18:19]
	s_or_b32 m0, s22, 0x400
	v_lshl_or_b32 v50, v2, 12, v53
	global_load_lds_dwordx4 v64, s[18:19]
	s_add_i32 m0, s22, 0x2000
	v_lshl_or_b32 v2, v3, 12, v52
	global_load_lds_dwordx4 v50, s[4:5]
	s_add_i32 m0, s22, 0x2400
	v_mov_b32_e32 v3, v51
	global_load_lds_dwordx4 v2, s[4:5]
	s_add_i32 m0, s22, 0x4000
	v_lshl_add_u64 v[60:61], s[4:5], 0, v[50:51]
	v_lshl_add_u64 v[62:63], s[4:5], 0, v[2:3]
	s_add_u32 s4, s18, 0x2000
	s_addc_u32 s5, s19, 0
	s_add_i32 m0, s22, 0x4400
	s_load_dwordx2 s[0:1], s[0:1], 0x20
	s_mov_b64 s[4:5], 0x80
	v_lshl_add_u64 v[2:3], v[60:61], 0, s[4:5]
	s_add_i32 m0, s22, 0x6000
	v_lshrrev_b32_e32 v4, 1, v0
	v_lshl_add_u64 v[2:3], v[62:63], 0, s[4:5]
	s_add_i32 m0, s22, 0x6400
	v_and_b32_e32 v5, 4, v4
	v_lshlrev_b32_e32 v3, 1, v0
	v_and_b32_e32 v2, 19, v0
	v_and_b32_e32 v3, 8, v3
	v_or3_b32 v2, v3, v2, v5
	s_waitcnt vmcnt(0)
	v_lshlrev_b32_e32 v115, 7, v2
	v_lshrrev_b32_e32 v3, 1, v2
	v_bfe_u32 v46, v2, 1, 3
	v_bitop3_b32 v2, v54, v4, 7 bitop3:0x78
	s_mov_b32 s3, 0
	v_lshlrev_b32_e32 v108, 3, v54
	s_mov_b32 s23, 1
	s_mov_b64 s[16:17], 0x2000
	v_lshlrev_b32_e32 v109, 7, v98
	v_lshlrev_b32_e32 v110, 4, v2
	s_movk_i32 s25, 0x400
	v_bfe_u32 v50, v0, 1, 3
	s_barrier
	s_and_b32 s29, s28, 7
	s_lshr_b32 s40, s28, 3
	s_lshr_b32 s41, s40, 5
	s_lshl_b32 s41, s41, 3
	s_or_b32 s29, s41, s29
	s_and_b32 s40, s40, 1
	s_lshl_b32 s29, s29, 18
	s_lshl_b32 s41, s40, 17
	s_lshl_b32 s42, s40, 11
	s_add_i32 s41, s41, s29
	s_add_i32 s41, s41, 0x6000
	s_add_i32 s42, s42, s29
	s_add_i32 s42, s42, 0x180
	v_and_b32_e32 v145, 63, v0
	v_lshrrev_b32_e32 v146, 3, v145
	v_lshl_add_u32 v146, s21, 4, v146
	v_and_b32_e32 v145, 7, v145
	v_bfe_u32 v147, v146, 1, 3
	v_xor_b32_e32 v148, v145, v147
	v_xor_b32_e32 v147, 4, v148
	v_lshlrev_b32_e32 v148, 4, v148
	v_lshlrev_b32_e32 v147, 4, v147
	v_lshl_add_u32 v145, v146, 7, v148
	v_lshl_add_u32 v149, v146, 7, v147
	v_add_u32_e32 v149, 0x400, v149
	v_lshl_add_u32 v148, v146, 12, v148
	v_lshl_add_u32 v147, v146, 12, v147
	v_add_u32_e32 v147, 0x8000, v147
	s_waitcnt lgkmcnt(0)
	s_add_u32 s36, s32, s41
	s_addc_u32 s37, s33, 0
	s_add_u32 s38, s34, s42
	s_addc_u32 s39, s35, 0
	s_sub_u32 s40, s36, 0x4000
	s_subb_u32 s41, s37, 0
	s_sub_u32 s42, s38, 0x100
	s_subb_u32 s43, s39, 0
	s_add_i32 m0, s22, 0x4000
	s_nop 0
	global_load_lds_dwordx4 v145, s[40:41]
	s_add_i32 m0, s22, 0x4400
	s_nop 0
	global_load_lds_dwordx4 v149, s[40:41]
	s_add_i32 m0, s22, 0x6000
	s_nop 0
	global_load_lds_dwordx4 v148, s[42:43]
	s_add_i32 m0, s22, 0x6400
	s_nop 0
	global_load_lds_dwordx4 v147, s[42:43]
	v_bitop3_b32 v2, v54, v3, 7 bitop3:0x78
	v_lshlrev_b32_e32 v116, 4, v2
	v_or_b32_e32 v6, v115, v116
	ds_read_b128 v[2:5], v6
	ds_read_b128 v[18:21], v6 offset:4096
	v_bitop3_b32 v6, v54, v46, 2 bitop3:0x36
	v_lshlrev_b32_e32 v117, 4, v6
	v_or_b32_e32 v6, v115, v117
	ds_read_b128 v[34:37], v6
	ds_read_b128 v[38:41], v6 offset:4096
	s_waitcnt vmcnt(4) lgkmcnt(0)
	v_mfma_f32_32x32x16_f16 v[2:17], v[2:5], v[94:97], 0
	v_bitop3_b32 v42, v54, v46, 4 bitop3:0x36
	v_bitop3_b32 v46, v54, v46, 6 bitop3:0x36
	v_lshlrev_b32_e32 v118, 4, v42
	v_lshlrev_b32_e32 v119, 4, v46
	v_or_b32_e32 v42, v115, v118
	v_or_b32_e32 v56, v115, v119
	v_mfma_f32_32x32x16_f16 v[18:33], v[18:21], v[94:97], 0
	v_mfma_f32_32x32x16_f16 v[2:17], v[34:37], v[90:93], v[2:17]
	ds_read_b128 v[34:37], v42
	ds_read_b128 v[42:45], v42 offset:4096
	ds_read_b128 v[46:49], v56
	ds_read_b128 v[56:59], v56 offset:4096
	v_mfma_f32_32x32x16_f16 v[18:33], v[38:41], v[90:93], v[18:33]
	s_waitcnt lgkmcnt(3)
	v_mfma_f32_32x32x16_f16 v[2:17], v[34:37], v[86:89], v[2:17]
	s_waitcnt lgkmcnt(2)
	v_mfma_f32_32x32x16_f16 v[18:33], v[42:45], v[86:89], v[18:33]
	s_waitcnt lgkmcnt(1)
	v_mfma_f32_32x32x16_f16 v[2:17], v[46:49], v[82:85], v[2:17]
	s_waitcnt lgkmcnt(0)
	v_mfma_f32_32x32x16_f16 v[18:33], v[56:59], v[82:85], v[18:33]
	s_add_i32 m0, s22, 0x8000
	s_add_u32 s18, s18, 0x4000
	s_addc_u32 s19, s19, 0
	global_load_lds_dwordx4 v55, s[18:19]
	s_add_i32 m0, s22, 0x8400
	s_nop 0
	global_load_lds_dwordx4 v64, s[18:19]
	s_mov_b64 s[18:19], 0x100
	v_lshl_add_u64 v[34:35], v[60:61], 0, s[18:19]
	s_add_i32 m0, s22, 0xa000
	s_nop 0
	global_load_lds_dwordx4 v[34:35], off
	v_lshl_add_u64 v[34:35], v[62:63], 0, s[18:19]
	s_add_i32 m0, s22, 0xa400
	s_mov_b32 s18, 0x8000
	global_load_lds_dwordx4 v[34:35], off
	v_max3_f32 v34, v2, v3, v4
	v_max3_f32 v34, v34, v5, v6
	v_max3_f32 v34, v34, v7, v8
	v_max3_f32 v34, v34, v9, v10
	v_max3_f32 v34, v34, v11, v12
	v_max3_f32 v34, v34, v13, v14
	v_max3_f32 v34, v34, v15, v16
	v_max_f32 v34, v34, v17
	v_max3_f32 v35, v18, v19, v20
	v_max3_f32 v35, v35, v21, v22
	v_max3_f32 v35, v35, v23, v24
	v_max3_f32 v35, v35, v25, v26
	v_max3_f32 v35, v35, v27, v28
	v_max3_f32 v35, v35, v29, v30
	v_max3_f32 v35, v35, v31, v32
	v_max_f32 v35, v35, v33
	s_nop 0
	v_max3_f32 v34, v34, v35, v35
	s_nop 0
	v_mov_b32_e32 v35, v34
	s_nop 1
	v_permlane32_swap_b32_e32 v34, v35
	v_max3_f32 v47, v34, v35, v35
	s_nop 0
	v_sub_f32_e32 v10, v10, v47
	v_exp_f32_e32 v126, v10
	v_bitop3_b32 v10, v54, v50, 2 bitop3:0x36
	v_sub_f32_e32 v6, v6, v47
	v_lshlrev_b32_e32 v112, 4, v10
	v_sub_f32_e32 v2, v2, v47
	v_sub_f32_e32 v3, v3, v47
	v_sub_f32_e32 v4, v4, v47
	v_sub_f32_e32 v5, v5, v47
	v_sub_f32_e32 v7, v7, v47
	v_sub_f32_e32 v8, v8, v47
	v_sub_f32_e32 v9, v9, v47
	v_exp_f32_e32 v106, v6
	v_or_b32_e32 v6, v109, v110
	v_or_b32_e32 v10, v109, v112
	v_sub_f32_e32 v19, v19, v47
	v_sub_f32_e32 v20, v20, v47
	v_sub_f32_e32 v21, v21, v47
	v_sub_f32_e32 v22, v22, v47
	v_exp_f32_e32 v80, v2
	v_exp_f32_e32 v100, v3
	v_exp_f32_e32 v102, v4
	v_exp_f32_e32 v104, v5
	v_exp_f32_e32 v120, v7
	v_exp_f32_e32 v122, v8
	v_exp_f32_e32 v124, v9
	ds_read_b128 v[2:5], v6 offset:8192
	ds_read_b128 v[6:9], v6 offset:12288
	ds_read_b128 v[56:59], v10 offset:8192
	ds_read_b128 v[60:63], v10 offset:12288
	v_exp_f32_e32 v101, v19
	v_exp_f32_e32 v103, v20
	v_exp_f32_e32 v105, v21
	v_exp_f32_e32 v107, v22
	v_sub_f32_e32 v34, 0, v47
	v_mov_b32_e32 v35, v34
	v_mov_b32_e32 v36, v34
	v_mov_b32_e32 v37, v34
	v_mov_b32_e32 v38, v34
	v_mov_b32_e32 v39, v34
	v_mov_b32_e32 v40, v34
	v_mov_b32_e32 v41, v34
	v_mov_b32_e32 v42, v34
	v_mov_b32_e32 v43, v34
	v_mov_b32_e32 v44, v34
	v_mov_b32_e32 v45, v34
	v_mov_b32_e32 v46, v34
	v_sub_f32_e32 v18, v18, v47
	v_sub_f32_e32 v23, v23, v47
	v_sub_f32_e32 v24, v24, v47
	v_sub_f32_e32 v25, v25, v47
	v_sub_f32_e32 v26, v26, v47
	v_sub_f32_e32 v27, v27, v47
	v_sub_f32_e32 v28, v28, v47
	v_sub_f32_e32 v29, v29, v47
	v_sub_f32_e32 v30, v30, v47
	v_sub_f32_e32 v31, v31, v47
	v_sub_f32_e32 v32, v32, v47
	v_sub_f32_e32 v33, v33, v47
	v_sub_f32_e32 v11, v11, v47
	v_sub_f32_e32 v12, v12, v47
	v_sub_f32_e32 v13, v13, v47
	v_sub_f32_e32 v14, v14, v47
	v_sub_f32_e32 v15, v15, v47
	v_sub_f32_e32 v16, v16, v47
	v_sub_f32_e32 v17, v17, v47
	v_mov_b32_e32 v47, v34
	v_mov_b32_e32 v48, v34
	v_mov_b32_e32 v49, v34
	v_exp_f32_e32 v128, v11
	v_exp_f32_e32 v130, v12
	v_exp_f32_e32 v132, v13
	v_exp_f32_e32 v134, v14
	v_exp_f32_e32 v136, v15
	v_exp_f32_e32 v138, v16
	v_exp_f32_e32 v140, v17
	v_exp_f32_e32 v81, v18
	v_exp_f32_e32 v121, v23
	v_exp_f32_e32 v123, v24
	v_exp_f32_e32 v125, v25
	v_exp_f32_e32 v127, v26
	v_exp_f32_e32 v129, v27
	v_exp_f32_e32 v131, v28
	v_exp_f32_e32 v133, v29
	v_exp_f32_e32 v135, v30
	v_exp_f32_e32 v137, v31
	v_exp_f32_e32 v139, v32
	v_exp_f32_e32 v141, v33
	v_cvt_pk_f16_f32 v13, v122, v124
	v_cvt_pk_f16_f32 v12, v106, v120
	v_cvt_pk_f16_f32 v11, v102, v104
	v_cvt_pk_f16_f32 v10, v80, v100
	v_cvt_pk_f16_f32 v67, v138, v140
	v_cvt_pk_f16_f32 v66, v134, v136
	s_waitcnt lgkmcnt(0)
	v_mfma_f32_32x32x16_f16 v[18:33], v[2:5], v[10:13], 0
	v_cvt_pk_f16_f32 v65, v130, v132
	v_cvt_pk_f16_f32 v64, v126, v128
	v_bitop3_b32 v55, v54, v50, 4 bitop3:0x36
	v_bitop3_b32 v50, v54, v50, 6 bitop3:0x36
	v_lshlrev_b32_e32 v111, 4, v55
	v_lshlrev_b32_e32 v113, 4, v50
	v_or_b32_e32 v55, v109, v111
	v_mfma_f32_32x32x16_f16 v[2:17], v[6:9], v[10:13], 0
	v_or_b32_e32 v50, v109, v113
	v_mfma_f32_32x32x16_f16 v[18:33], v[56:59], v[64:67], v[18:33]
	ds_read_b128 v[56:59], v55 offset:8192
	ds_read_b128 v[68:71], v55 offset:12288
	ds_read_b128 v[72:75], v50 offset:8192
	ds_read_b128 v[76:79], v50 offset:12288
	v_mfma_f32_32x32x16_f16 v[2:17], v[60:63], v[64:67], v[2:17]
	v_add_f32_e64 v54, v80, 0
	v_add_f32_e64 v55, v81, 0
	v_cvt_pk_f16_f32 v63, v123, v125
	v_add_f32_e64 v54, v54, v100
	v_add_f32_e64 v55, v55, v101
	v_cvt_pk_f16_f32 v62, v107, v121
	v_add_f32_e32 v54, v54, v102
	v_add_f32_e32 v55, v55, v103
	v_cvt_pk_f16_f32 v61, v103, v105
	v_add_f32_e32 v54, v54, v104
	v_add_f32_e32 v55, v55, v105
	v_cvt_pk_f16_f32 v60, v81, v101
	v_add_f32_e32 v54, v54, v106
	v_add_f32_e32 v55, v55, v107
	v_cvt_pk_f16_f32 v67, v139, v141
	v_add_f32_e32 v54, v54, v120
	v_add_f32_e32 v55, v55, v121
	s_waitcnt lgkmcnt(0)
	v_mfma_f32_32x32x16_f16 v[18:33], v[56:59], v[60:63], v[18:33]
	v_add_f32_e64 v54, v54, v122
	v_add_f32_e64 v55, v55, v123
	v_cvt_pk_f16_f32 v66, v135, v137
	v_add_f32_e64 v54, v54, v124
	v_add_f32_e64 v55, v55, v125
	v_cvt_pk_f16_f32 v65, v131, v133
	v_add_f32_e32 v54, v54, v126
	v_add_f32_e32 v55, v55, v127
	v_cvt_pk_f16_f32 v64, v127, v129
	v_add_f32_e32 v54, v54, v128
	v_add_f32_e32 v55, v55, v129
	v_mfma_f32_32x32x16_f16 v[2:17], v[68:71], v[60:63], v[2:17]
	v_add_f32_e64 v54, v54, v130
	v_add_f32_e64 v55, v55, v131
	s_add_u32 s8, s8, s24
	v_add_f32_e64 v54, v54, v132
	v_add_f32_e64 v55, v55, v133
	s_addc_u32 s9, s9, 0
	v_add_f32_e32 v54, v54, v134
	v_add_f32_e32 v55, v55, v135
	s_mov_b64 s[26:27], 0x180
	v_add_f32_e32 v54, v54, v136
	v_add_f32_e32 v55, v55, v137
	v_mfma_f32_32x32x16_f16 v[18:33], v[72:75], v[64:67], v[18:33]
	v_add_f32_e64 v54, v54, v138
	v_add_f32_e64 v55, v55, v139
	v_add_f32_e64 v54, v54, v140
	v_add_f32_e64 v55, v55, v141
	v_add_f32_e32 v50, v54, v55
	v_add_f32_e32 v114, 0, v50
	v_lshlrev_b32_e32 v50, 12, v1
	v_lshl_or_b32 v56, s21, 16, v50
	v_mfma_f32_32x32x16_f16 v[2:17], v[76:79], v[64:67], v[2:17]
	v_or_b32_e32 v50, v56, v53
	v_lshl_add_u64 v[54:55], s[8:9], 0, v[50:51]
	v_or3_b32 v50, v56, v52, s18
	v_lshl_add_u64 v[100:101], v[54:55], 0, s[26:27]
	v_lshl_add_u64 v[54:55], s[8:9], 0, v[50:51]
	s_lshl_b32 s8, s20, 17
	v_lshl_or_b32 v56, v1, 7, s22
	s_add_u32 s6, s6, s8
	v_or_b32_e32 v50, v56, v53
	s_addc_u32 s7, s7, 0
	v_lshl_add_u64 v[102:103], v[54:55], 0, s[26:27]
	v_lshl_add_u64 v[54:55], s[6:7], 0, v[50:51]
	v_or3_b32 v50, v56, v52, s25
	s_mov_b64 s[8:9], 0x6000
	v_lshl_add_u64 v[50:51], s[6:7], 0, v[50:51]
	v_lshl_add_u64 v[104:105], v[54:55], 0, s[8:9]
	v_lshl_add_u64 v[106:107], v[50:51], 0, s[8:9]
	s_mov_b32 s8, 0x46000000
	s_mov_b32 s9, 1
